# FIN: next-row loads no longer waited/unpacked right after issue (unpack at row end replaces plain copies); explicit waits for the first inv word and class-change vectors
# baseline (speedup 1.0000x reference)
.LBB0_1566:
	v_mbcnt_lo_u32_b32 v0, -1, 0
	v_mbcnt_hi_u32_b32 v0, -1, v0
	s_mov_b32 s1, 0
	v_lshl_add_u32 v0, s86, 6, v0
	s_add_i32 s1, s1, 0x25f98
	v_mov_b32_e32 v1, s1
	s_mov_b32 s1, 0
	ds_read_b64 v[2:3], v1
	s_add_i32 s1, s1, 0x25f00
	v_mov_b32_e32 v1, s1
	s_mov_b32 s1, 0
	ds_read_b64 v[4:5], v1
	s_add_i32 s1, s1, 0x25f10
	v_mov_b32_e32 v1, s1
	s_mov_b32 s1, 0
	s_waitcnt lgkmcnt(0)
	ds_read_b64 v[4:5], v1
	s_add_i32 s1, s1, 0x25f88
	s_mov_b32 s0, 0
	v_mov_b32_e32 v1, s1
	s_waitcnt lgkmcnt(0)
	ds_read_b64 v[4:5], v1
	s_add_i32 s0, s0, 0x25f90
	v_mov_b32_e32 v1, s0
	ds_read_b64 v[6:7], v1
	v_readfirstlane_b32 s2, v0
	s_ashr_i32 s2, s2, 6
	v_readlane_b32 s3, v243, 2
	s_add_i32 s14, s2, s3
	v_readfirstlane_b32 s0, v2
	v_readfirstlane_b32 s1, v3
	s_waitcnt lgkmcnt(1)
	v_readfirstlane_b32 s8, v4
	v_readfirstlane_b32 s9, v5
	s_waitcnt lgkmcnt(0)
	v_readfirstlane_b32 s6, v6
	s_cmpk_gt_i32 s14, 0x7fff
	v_readfirstlane_b32 s7, v7
	s_cbranch_scc1 .LBB0_1579
	s_add_u32 s2, s0, 0x70000000
	s_addc_u32 s3, s1, 0
	s_add_u32 s15, s0, 0x6ff44000
	s_addc_u32 s16, s1, 0
	s_add_u32 s10, s0, 0x33400000
	s_addc_u32 s11, s1, 0
	s_ashr_i32 s4, s14, 14
	s_mulk_i32 s4, 0x4100
	s_and_b32 s5, s14, 0x3fff
	s_add_i32 s4, s5, s4
	s_addk_i32 s4, 0x100
	s_ashr_i32 s5, s4, 31
	s_lshl_b64 s[12:13], s[4:5], 11
	v_lshlrev_b32_e32 v2, 2, v0
	v_and_b32_e32 v91, 15, v0
	s_add_u32 s12, s10, s12
	v_and_b32_e32 v48, 0xfc, v2
	v_lshl_or_b32 v0, s4, 4, v91
	s_addc_u32 s13, s11, s13
	v_lshlrev_b32_e32 v28, 1, v48
	v_ashrrev_i32_e32 v1, 31, v0
	global_load_dwordx2 v[30:31], v28, s[12:13]
	global_load_dwordx2 v[32:33], v28, s[12:13] offset:512
	global_load_dwordx2 v[34:35], v28, s[12:13] offset:1024
	global_load_dwordx2 v[36:37], v28, s[12:13] offset:1536
	v_lshl_add_u64 v[0:1], v[0:1], 2, s[2:3]
	global_load_dword v99, v[0:1], off
	v_mov_b32_e32 v49, 0
	v_bfrev_b32_e32 v0, 0.5
	s_movk_i32 s19, 0x80
	v_mov_b32_e32 v29, v49
	v_mov_b32_e32 v12, v49
	v_mov_b32_e32 v13, v49
	v_mov_b32_e32 v14, v49
	v_mov_b32_e32 v15, v49
	s_mov_b64 s[12:13], 0x5d000000
	v_mov_b32_e32 v39, v49
	v_bitop3_b32 v93, v2, 4, v0 bitop3:0x6c
	v_bitop3_b32 v94, v2, 8, v0 bitop3:0x6c
	v_bitop3_b32 v95, v2, 16, v0 bitop3:0x6c
	v_bitop3_b32 v96, v2, 32, v0 bitop3:0x6c
	v_bitop3_b32 v97, v2, 64, v0 bitop3:0x6c
	v_bitop3_b32 v98, v2, s19, v0 bitop3:0x6c
	v_lshlrev_b32_e32 v38, 2, v48
	v_lshl_add_u64 v[40:41], s[0:1], 0, v[48:49]
	v_mov_b64_e32 v[18:19], v[14:15]
	v_mov_b64_e32 v[22:23], v[14:15]
	v_mov_b64_e32 v[26:27], v[14:15]
	v_mov_b64_e32 v[0:1], v[12:13]
	v_mov_b64_e32 v[4:5], v[12:13]
	v_mov_b64_e32 v[8:9], v[12:13]
	v_lshl_add_u64 v[56:57], s[10:11], 0, v[28:29]
	s_mov_b32 s18, -1
	s_mov_b64 s[4:5], 0x43b000
	v_mov_b32_e32 v92, 0x358637bd
	s_movk_i32 s17, 0x3f00
	v_lshlrev_b32_e32 v48, 2, v48
	v_mov_b64_e32 v[16:17], v[12:13]
	v_mov_b64_e32 v[20:21], v[12:13]
	v_mov_b64_e32 v[24:25], v[12:13]
	v_mov_b64_e32 v[2:3], v[14:15]
	v_mov_b64_e32 v[6:7], v[14:15]
	v_mov_b64_e32 v[10:11], v[14:15]
	v_lshl_add_u64 v[50:51], s[8:9], 0, v[38:39]
	v_lshl_add_u64 v[52:53], v[40:41], 0, s[12:13]
	v_lshl_add_u64 v[54:55], s[6:7], 0, v[38:39]
	s_waitcnt vmcnt(4)
	v_lshlrev_b32_e32 v66, 16, v30
	v_and_b32_e32 v67, 0xffff0000, v30
	v_lshlrev_b32_e32 v72, 16, v31
	v_and_b32_e32 v73, 0xffff0000, v31
	v_mov_b64_e32 v[30:31], v[14:15]
	s_waitcnt vmcnt(3)
	v_lshlrev_b32_e32 v62, 16, v32
	v_and_b32_e32 v63, 0xffff0000, v32
	v_lshlrev_b32_e32 v70, 16, v33
	v_and_b32_e32 v71, 0xffff0000, v33
	s_waitcnt vmcnt(2)
	v_lshlrev_b32_e32 v60, 16, v34
	v_and_b32_e32 v61, 0xffff0000, v34
	v_lshlrev_b32_e32 v68, 16, v35
	v_and_b32_e32 v69, 0xffff0000, v35
	s_waitcnt vmcnt(1)
	v_lshlrev_b32_e32 v58, 16, v36
	v_and_b32_e32 v59, 0xffff0000, v36
	v_lshlrev_b32_e32 v64, 16, v37
	v_and_b32_e32 v65, 0xffff0000, v37
	v_mov_b64_e32 v[28:29], v[12:13]
	s_waitcnt vmcnt(0)
	s_branch .LBB0_1570

.LBB0_1569:
	v_pk_fma_f32 v[72:73], v[14:15], v[88:89], v[72:73]
	v_pk_fma_f32 v[66:67], v[12:13], v[86:87], v[66:67]
	v_pk_fma_f32 v[78:79], v[20:21], v[78:79], v[60:61]
	v_pk_fma_f32 v[74:75], v[24:25], v[74:75], v[58:59]
	v_pk_mul_f32 v[58:59], v[72:73], v[72:73]
	v_pk_mul_f32 v[60:61], v[66:67], v[66:67]
	v_pk_fma_f32 v[64:65], v[26:27], v[76:77], v[64:65]
	v_pk_mov_b32 v[76:77], v[60:61], v[58:59] op_sel:[1,0]
	v_mov_b32_e32 v61, v59
	v_pk_fma_f32 v[70:71], v[18:19], v[84:85], v[70:71]
	v_pk_fma_f32 v[62:63], v[16:17], v[82:83], v[62:63]
	v_pk_add_f32 v[58:59], v[76:77], v[60:61]
	v_pk_mul_f32 v[60:61], v[70:71], v[70:71]
	v_pk_add_f32 v[58:59], v[58:59], v[58:59] op_sel_hi:[0,1]
	v_pk_mul_f32 v[76:77], v[62:63], v[62:63]
	v_pk_fma_f32 v[68:69], v[22:23], v[80:81], v[68:69]
	v_pk_mov_b32 v[80:81], v[76:77], v[60:61] op_sel:[1,0]
	v_mov_b32_e32 v77, v61
	v_mul_f32_e32 v58, v78, v78
	v_pk_add_f32 v[60:61], v[80:81], v[76:77]
	v_pk_fma_f32 v[76:77], v[78:79], v[78:79], v[58:59] op_sel_hi:[1,1,0]
	v_mul_f32_e32 v58, v68, v68
	v_pk_add_f32 v[60:61], v[60:61], v[60:61] op_sel_hi:[0,1]
	v_pk_fma_f32 v[80:81], v[68:69], v[68:69], v[58:59] op_sel_hi:[1,1,0]
	v_mul_f32_e32 v76, v74, v74
	v_mul_f32_e32 v80, v75, v75
	v_mul_f32_e32 v58, v64, v64
	v_mul_f32_e32 v60, v65, v65
	v_pk_add_f32 v[76:77], v[76:77], v[80:81]
	v_pk_add_f32 v[58:59], v[58:59], v[60:61]
	s_and_b64 s[8:9], s[8:9], exec
	v_pk_add_f32 v[58:59], v[76:77], v[58:59]
	s_cselect_b32 s8, s17, 0xffffff00
	v_add_f32_e32 v58, v58, v59
	ds_bpermute_b32 v59, v93, v58
	s_add_i32 s8, s19, s8
	s_ashr_i32 s9, s8, 31
	s_lshl_b64 s[8:9], s[8:9], 12
	v_lshl_add_u64 v[80:81], v[54:55], 0, s[8:9]
	s_waitcnt lgkmcnt(0)
	v_add_f32_e32 v58, v58, v59
	ds_bpermute_b32 v59, v94, v58
	s_and_b64 vcc, exec, s[6:7]
	s_waitcnt vmcnt(0)
	v_mov_b32_e32 v99, v100
	s_waitcnt lgkmcnt(0)
	v_add_f32_e32 v58, v58, v59
	ds_bpermute_b32 v59, v95, v58
	s_waitcnt lgkmcnt(0)
	v_add_f32_e32 v58, v58, v59
	ds_bpermute_b32 v59, v96, v58
	s_waitcnt lgkmcnt(0)
	v_add_f32_e32 v58, v58, v59
	ds_bpermute_b32 v59, v97, v58
	s_waitcnt lgkmcnt(0)
	v_add_f32_e32 v58, v58, v59
	ds_bpermute_b32 v59, v98, v58
	s_waitcnt lgkmcnt(0)
	v_add_f32_e32 v58, v58, v59
	v_fmamk_f32 v58, v58, 0x3a800000, v92
	v_rsq_f32_e32 v76, v58
	s_nop 0
	v_pk_mul_f32 v[58:59], v[66:67], v[76:77] op_sel_hi:[1,0]
	v_pk_mul_f32 v[60:61], v[72:73], v[76:77] op_sel_hi:[1,0]
	v_pk_mul_f32 v[58:59], v[0:1], v[58:59]
	v_pk_mul_f32 v[60:61], v[2:3], v[60:61]
	global_store_dwordx4 v[80:81], v[58:61], off nt
	v_lshlrev_b32_e32 v66, 16, v140
	v_and_b32_e32 v67, 0xffff0000, v140
	v_pk_mul_f32 v[58:59], v[62:63], v[76:77] op_sel_hi:[1,0]
	v_pk_mul_f32 v[60:61], v[70:71], v[76:77] op_sel_hi:[1,0]
	v_pk_mul_f32 v[58:59], v[4:5], v[58:59]
	v_pk_mul_f32 v[60:61], v[6:7], v[60:61]
	global_store_dwordx4 v[80:81], v[58:61], off offset:1024 nt
	v_lshlrev_b32_e32 v72, 16, v141
	v_and_b32_e32 v73, 0xffff0000, v141
	v_pk_mul_f32 v[58:59], v[78:79], v[76:77] op_sel_hi:[1,0]
	v_pk_mul_f32 v[60:61], v[68:69], v[76:77] op_sel_hi:[1,0]
	v_pk_mul_f32 v[58:59], v[8:9], v[58:59]
	v_pk_mul_f32 v[60:61], v[10:11], v[60:61]
	global_store_dwordx4 v[80:81], v[58:61], off offset:2048 nt
	v_lshlrev_b32_e32 v62, 16, v142
	v_and_b32_e32 v63, 0xffff0000, v142
	v_pk_mul_f32 v[58:59], v[74:75], v[76:77] op_sel_hi:[1,0]
	v_pk_mul_f32 v[60:61], v[64:65], v[76:77] op_sel_hi:[1,0]
	v_pk_mul_f32 v[58:59], v[28:29], v[58:59]
	v_pk_mul_f32 v[60:61], v[30:31], v[60:61]
	global_store_dwordx4 v[80:81], v[58:61], off offset:3072 nt
	v_lshlrev_b32_e32 v70, 16, v143
	v_and_b32_e32 v71, 0xffff0000, v143
	v_lshlrev_b32_e32 v60, 16, v144
	v_and_b32_e32 v61, 0xffff0000, v144
	v_lshlrev_b32_e32 v68, 16, v145
	v_and_b32_e32 v69, 0xffff0000, v145
	v_lshlrev_b32_e32 v58, 16, v146
	v_and_b32_e32 v59, 0xffff0000, v146
	v_lshlrev_b32_e32 v64, 16, v147
	v_and_b32_e32 v65, 0xffff0000, v147
	s_cbranch_vccnz .LBB0_1579
.LBB0_1570:
	s_ashr_i32 s6, s14, 14
	s_mulk_i32 s6, 0x4100
	s_and_b32 s7, s14, 0x3fff
	s_add_i32 s6, s7, s6
	s_add_i32 s10, s6, 0x100
	s_cmpk_gt_i32 s10, 0x40ff
	s_cselect_b64 s[8:9], -1, 0
	s_and_b64 s[6:7], s[8:9], exec
	s_cselect_b32 s19, 0xffffbf00, 0
	v_cndmask_b32_e64 v74, 0, 1, s[8:9]
	s_add_i32 s19, s19, s10
	s_cmpk_gt_i32 s19, 0xff
	v_readfirstlane_b32 s6, v74
	s_cselect_b32 s6, s6, 2
	s_cmp_eq_u32 s6, s18
	s_cbranch_scc1 .LBB0_1572
	s_mul_i32 s7, s6, 0x6000
	s_add_u32 s10, s0, s7
	s_addc_u32 s11, s1, 0
	v_lshl_add_u64 v[12:13], s[10:11], 0, v[48:49]
	v_lshl_add_u64 v[74:75], v[12:13], 0, s[4:5]
	v_add_co_u32_e32 v76, vcc, 0x43b000, v12
	global_load_dwordx4 v[0:3], v[50:51], off
	global_load_dwordx4 v[4:7], v[50:51], off offset:1024
	global_load_dwordx4 v[8:11], v[50:51], off offset:2048
	global_load_dwordx4 v[28:31], v[50:51], off offset:3072
	v_addc_co_u32_e32 v77, vcc, 0, v13, vcc
	global_load_dwordx4 v[16:19], v[74:75], off offset:1024
	global_load_dwordx4 v[20:23], v[74:75], off offset:2048
	global_load_dwordx4 v[12:15], v[76:77], off
	global_load_dwordx4 v[24:27], v[74:75], off offset:3072
	s_waitcnt vmcnt(0)
	s_mov_b32 s18, s6
.LBB0_1572:
	s_add_i32 s14, s14, s80
	s_cmpk_gt_i32 s14, 0x7fff
	s_cselect_b64 s[6:7], -1, 0
	s_and_b64 vcc, exec, s[6:7]
	s_cbranch_vccnz .LBB0_1574
	s_ashr_i32 s10, s14, 14
	s_mulk_i32 s10, 0x4100
	s_and_b32 s11, s14, 0x3fff
	s_add_i32 s10, s11, s10
	s_addk_i32 s10, 0x100
	s_ashr_i32 s11, s10, 31
	s_lshl_b64 s[12:13], s[10:11], 11
	v_lshl_add_u64 v[32:33], v[56:57], 0, s[12:13]
	global_load_dwordx2 v[140:141], v[32:33], off
	global_load_dwordx2 v[142:143], v[32:33], off offset:512
	global_load_dwordx2 v[144:145], v[32:33], off offset:1024
	global_load_dwordx2 v[146:147], v[32:33], off offset:1536
	v_lshl_or_b32 v32, s10, 4, v91
	v_ashrrev_i32_e32 v33, 31, v32
	v_lshl_add_u64 v[32:33], v[32:33], 2, s[2:3]
	global_load_dword v100, v[32:33], off
	v_cmp_lt_i32_e32 vcc, -1, v99
	s_and_b32 s10, vcc_lo, 0xffff
	s_cmp_eq_u32 s10, 0
	s_cbranch_scc0 .LBB0_1575
	s_branch .LBB0_1568
